# v17 + non-temporal hint on the mLSTM A/C unit loads
# baseline (speedup 1.0000x reference)
.LBB0_396:
	v_mov_b32_e32 v74, v0
	v_mov_b32_e32 v26, v0
	s_mov_b32 s2, 6
	s_ashr_i32 s3, s2, 31
	s_lshl_b64 s[2:3], s[2:3], 3
	s_add_u32 s64, s0, s2
	s_mov_b32 s2, 7
	s_addc_u32 s65, s1, s3
	s_ashr_i32 s3, s2, 31
	s_lshl_b64 s[2:3], s[2:3], 3
	s_add_u32 s66, s0, s2
	s_addc_u32 s67, s1, s3
	s_lshl_b32 s2, s62, 4
	s_and_b32 s63, s2, 0xfffff800
	s_lshl_b32 s2, s62, 6
	s_and_b32 s9, s2, 0x7c0
	v_and_b32_e32 v27, 63, v26
	s_bfe_u32 s81, s62, 0x20005
	s_or_b32 s82, s63, s9
	v_cmp_ne_u32_e64 s[2:3], 1, v68
	s_andn2_b64 vcc, exec, s[10:11]
	v_mov_b32_e32 v3, 0
	v_mov_b32_e32 v1, 0
	s_cbranch_vccnz .LBB0_398
	v_or_b32_e32 v2, s82, v27
	v_ashrrev_i32_e32 v3, 31, v2
	v_lshlrev_b64 v[2:3], 5, v[2:3]
	v_lshl_add_u64 v[2:3], s[12:13], 0, v[2:3]
	s_lshl_b32 s58, s81, 2
	v_lshl_add_u64 v[2:3], v[2:3], 0, s[58:59]
	global_load_dword v1, v[2:3], off nt
	s_nop 0
	global_load_dword v3, v[2:3], off offset:16 nt
.LBB0_398:
	s_load_dwordx2 s[64:65], s[64:65], 0x0
	s_nop 0
	s_load_dwordx2 s[66:67], s[66:67], 0x0
	v_lshlrev_b32_e32 v17, 1, v74
	v_lshlrev_b32_e32 v2, 3, v74
	v_and_b32_e32 v16, 0x7e, v17
	v_and_b32_e32 v2, 0x200, v2
	s_lshl_b32 s8, s81, 7
	v_or3_b32 v14, s8, v2, v16
	v_lshlrev_b32_e32 v66, 2, v14
	s_waitcnt lgkmcnt(0)
	v_lshl_add_u64 v[8:9], s[64:65], 0, v[66:67]
	v_add_co_u32_e32 v6, vcc, s69, v8
	v_ashrrev_i32_e32 v28, 3, v74
	s_nop 0
	v_addc_co_u32_e32 v7, vcc, 0, v9, vcc
	v_add_co_u32_e32 v10, vcc, 0x3000, v8
	global_load_dwordx2 v[4:5], v[6:7], off offset:-4096 nt
	s_nop 0
	global_load_dwordx2 v[6:7], v[6:7], off nt
	v_addc_co_u32_e32 v11, vcc, 0, v9, vcc
	global_load_dwordx2 v[8:9], v66, s[64:65] nt
	global_load_dwordx2 v[12:13], v66, s[66:67] nt
	s_nop 0
	global_load_dwordx2 v[10:11], v[10:11], off nt
	v_and_b32_e32 v2, -16, v28
	v_readlane_b32 s64, v252, 12
	v_add_u32_e32 v18, s9, v2
	v_lshlrev_b32_e32 v66, 1, v14
	v_readlane_b32 s65, v252, 13
	s_add_i32 s9, s63, -3
	v_cmp_lt_i32_e32 vcc, 2, v18
	v_lshl_add_u64 v[14:15], s[64:65], 0, v[66:67]
	v_mov_b32_e32 v23, 0
	v_mov_b32_e32 v24, 0
	s_and_saveexec_b64 s[64:65], vcc
	s_cbranch_execz .LBB0_400
	v_add_u32_e32 v19, s9, v18
	v_mad_i64_i32 v[20:21], s[66:67], v19, s70, v[14:15]
	global_load_dword v24, v[20:21], off nt
.LBB0_400:
	s_or_b64 exec, exec, s[64:65]
	v_cmp_lt_i32_e32 vcc, 1, v18
	s_and_saveexec_b64 s[64:65], vcc
	s_cbranch_execz .LBB0_402
	v_add3_u32 v19, v18, s9, 1
	v_mad_i64_i32 v[20:21], s[66:67], v19, s70, v[14:15]
	global_load_dword v23, v[20:21], off nt
.LBB0_402:
	s_or_b64 exec, exec, s[64:65]
	v_mov_b32_e32 v19, 0
	v_cmp_lt_i32_e32 vcc, 0, v18
	v_mov_b32_e32 v21, 0
	s_and_saveexec_b64 s[64:65], vcc
	s_cbranch_execz .LBB0_404
	v_add_u32_e32 v20, s9, v18
	v_or_b32_e32 v20, 2, v20
	v_mad_i64_i32 v[20:21], s[66:67], v20, s70, v[14:15]
	global_load_dword v21, v[20:21], off nt
.LBB0_404:
	s_or_b64 exec, exec, s[64:65]
	v_cmp_lt_i32_e32 vcc, -1, v18
	s_and_saveexec_b64 s[64:65], vcc
	s_cbranch_execz .LBB0_406
	v_add_u32_e32 v19, s63, v18
	v_mad_i64_i32 v[30:31], s[66:67], v19, s70, v[14:15]
	global_load_dword v19, v[30:31], off nt
.LBB0_406:
	s_or_b64 exec, exec, s[64:65]
	v_mov_b32_e32 v44, 0
	v_mov_b32_e32 v45, 0
	s_and_saveexec_b64 s[64:65], vcc
	s_cbranch_execz .LBB0_408
	v_add3_u32 v20, v18, s9, 4
	v_mad_i64_i32 v[30:31], s[66:67], v20, s70, v[14:15]
	global_load_dword v45, v[30:31], off nt
.LBB0_408:
	s_or_b64 exec, exec, s[64:65]
	s_and_saveexec_b64 s[64:65], vcc
	s_cbranch_execz .LBB0_410
	v_add3_u32 v20, v18, s9, 5
	v_mad_i64_i32 v[30:31], s[66:67], v20, s70, v[14:15]
	global_load_dword v44, v[30:31], off nt
.LBB0_410:
	s_or_b64 exec, exec, s[64:65]
	v_mov_b32_e32 v42, 0
	v_mov_b32_e32 v43, 0
	s_and_saveexec_b64 s[64:65], vcc
	s_cbranch_execz .LBB0_412
	v_add3_u32 v20, v18, s9, 6
	v_mad_i64_i32 v[30:31], s[66:67], v20, s70, v[14:15]
	global_load_dword v43, v[30:31], off nt
.LBB0_412:
	s_or_b64 exec, exec, s[64:65]
	s_and_saveexec_b64 s[64:65], vcc
	s_cbranch_execz .LBB0_414
	v_add3_u32 v20, v18, s9, 7
	v_mad_i64_i32 v[30:31], s[66:67], v20, s70, v[14:15]
	global_load_dword v42, v[30:31], off nt
.LBB0_414:
	s_or_b64 exec, exec, s[64:65]
	v_mov_b32_e32 v40, 0
	v_mov_b32_e32 v41, 0
	s_and_saveexec_b64 s[64:65], vcc
	s_cbranch_execz .LBB0_416
	v_add3_u32 v20, v18, s9, 8
	v_mad_i64_i32 v[30:31], s[66:67], v20, s70, v[14:15]
	global_load_dword v41, v[30:31], off nt
.LBB0_416:
	s_or_b64 exec, exec, s[64:65]
	s_and_saveexec_b64 s[64:65], vcc
	s_cbranch_execz .LBB0_418
	v_add3_u32 v20, v18, s9, 9
	v_mad_i64_i32 v[30:31], s[66:67], v20, s70, v[14:15]
	global_load_dword v40, v[30:31], off nt
.LBB0_418:
	s_or_b64 exec, exec, s[64:65]
	v_mov_b32_e32 v38, 0
	v_mov_b32_e32 v39, 0
	s_and_saveexec_b64 s[64:65], vcc
	s_cbranch_execz .LBB0_420
	v_add3_u32 v20, v18, s9, 10
	v_mad_i64_i32 v[30:31], s[66:67], v20, s70, v[14:15]
	global_load_dword v39, v[30:31], off nt
.LBB0_420:
	s_or_b64 exec, exec, s[64:65]
	s_and_saveexec_b64 s[64:65], vcc
	s_cbranch_execz .LBB0_422
	v_add3_u32 v20, v18, s9, 11
	v_mad_i64_i32 v[30:31], s[66:67], v20, s70, v[14:15]
	global_load_dword v38, v[30:31], off nt
.LBB0_422:
	s_or_b64 exec, exec, s[64:65]
	v_mov_b32_e32 v36, 0
	v_mov_b32_e32 v37, 0
	s_and_saveexec_b64 s[64:65], vcc
	s_cbranch_execz .LBB0_424
	v_add3_u32 v20, v18, s9, 12
	v_mad_i64_i32 v[30:31], s[66:67], v20, s70, v[14:15]
	global_load_dword v37, v[30:31], off nt
.LBB0_424:
	s_or_b64 exec, exec, s[64:65]
	s_and_saveexec_b64 s[64:65], vcc
	s_cbranch_execz .LBB0_426
	v_add3_u32 v20, v18, s9, 13
	v_mad_i64_i32 v[30:31], s[66:67], v20, s70, v[14:15]
	global_load_dword v36, v[30:31], off nt
.LBB0_426:
	s_or_b64 exec, exec, s[64:65]
	v_mov_b32_e32 v34, 0
	v_mov_b32_e32 v35, 0
	s_and_saveexec_b64 s[64:65], vcc
	s_cbranch_execz .LBB0_428
	v_add3_u32 v20, v18, s9, 14
	v_mad_i64_i32 v[30:31], s[66:67], v20, s70, v[14:15]
	global_load_dword v35, v[30:31], off nt
.LBB0_428:
	s_or_b64 exec, exec, s[64:65]
	s_and_saveexec_b64 s[64:65], vcc
	s_cbranch_execz .LBB0_430
	v_add3_u32 v20, v18, s9, 15
	v_mad_i64_i32 v[30:31], s[66:67], v20, s70, v[14:15]
	global_load_dword v34, v[30:31], off nt
.LBB0_430:
	s_or_b64 exec, exec, s[64:65]
	v_cmp_lt_i32_e32 vcc, -14, v18
	v_mov_b32_e32 v32, 0
	v_mov_b32_e32 v33, 0
	s_and_saveexec_b64 s[64:65], vcc
	s_cbranch_execz .LBB0_432
	v_add3_u32 v20, v18, s9, 16
	v_mad_i64_i32 v[30:31], s[66:67], v20, s70, v[14:15]
	global_load_dword v33, v[30:31], off nt
.LBB0_432:
	s_or_b64 exec, exec, s[64:65]
	v_cmp_lt_i32_e32 vcc, -15, v18
	s_and_saveexec_b64 s[64:65], vcc
	s_cbranch_execz .LBB0_434
	v_add3_u32 v20, v18, s9, 17
	v_mad_i64_i32 v[30:31], s[66:67], v20, s70, v[14:15]
	global_load_dword v32, v[30:31], off nt
.LBB0_434:
	s_or_b64 exec, exec, s[64:65]
	v_cmp_lt_i32_e32 vcc, -16, v18
	v_mov_b32_e32 v30, 0
	s_and_saveexec_b64 s[64:65], vcc
	s_cbranch_execz .LBB0_436
	v_add3_u32 v18, v18, s9, 18
	v_mad_i64_i32 v[14:15], s[66:67], v18, s70, v[14:15]
	global_load_dword v30, v[14:15], off nt
.LBB0_436:
	s_or_b64 exec, exec, s[64:65]
	v_readlane_b32 s64, v252, 12
	v_readlane_b32 s65, v252, 13
	s_lshl_b32 s66, s81, 9
	s_nop 3
	s_add_u32 s64, s64, s66
	s_addc_u32 s65, s65, 0
	v_lshlrev_b32_e32 v158, 2, v0
	v_and_b32_e32 v158, 0x1fc, v158
	v_mov_b32_e32 v159, 0
	v_lshl_add_u64 v[160:161], s[64:65], 0, v[158:159]
	v_ashrrev_i32_e32 v158, 3, v0
	v_and_b32_e32 v158, -16, v158
	v_add_u32_e32 v158, s82, v158
	v_mad_i64_i32 v[162:163], s[64:65], v158, s70, v[160:161]
	s_mov_b32 s66, 0x3000
	s_mov_b32 s67, 0
	global_load_dword v142, v[162:163], off offset:2048 nt
	v_lshl_add_u64 v[162:163], v[162:163], 0, s[66:67]
	global_load_dword v143, v[162:163], off offset:2048 nt
	v_lshl_add_u64 v[162:163], v[162:163], 0, s[66:67]
	global_load_dword v144, v[162:163], off offset:2048 nt
	v_lshl_add_u64 v[162:163], v[162:163], 0, s[66:67]
	global_load_dword v145, v[162:163], off offset:2048 nt
	v_lshl_add_u64 v[162:163], v[162:163], 0, s[66:67]
	global_load_dword v146, v[162:163], off offset:2048 nt
	v_lshl_add_u64 v[162:163], v[162:163], 0, s[66:67]
	global_load_dword v147, v[162:163], off offset:2048 nt
	v_lshl_add_u64 v[162:163], v[162:163], 0, s[66:67]
	global_load_dword v148, v[162:163], off offset:2048 nt
	v_lshl_add_u64 v[162:163], v[162:163], 0, s[66:67]
	global_load_dword v149, v[162:163], off offset:2048 nt
	v_lshl_add_u64 v[162:163], v[162:163], 0, s[66:67]
	global_load_dword v150, v[162:163], off offset:2048 nt
	v_lshl_add_u64 v[162:163], v[162:163], 0, s[66:67]
	global_load_dword v151, v[162:163], off offset:2048 nt
	v_lshl_add_u64 v[162:163], v[162:163], 0, s[66:67]
	global_load_dword v152, v[162:163], off offset:2048 nt
	v_lshl_add_u64 v[162:163], v[162:163], 0, s[66:67]
	global_load_dword v153, v[162:163], off offset:2048 nt
	v_lshl_add_u64 v[162:163], v[162:163], 0, s[66:67]
	global_load_dword v154, v[162:163], off offset:2048 nt
	v_lshl_add_u64 v[162:163], v[162:163], 0, s[66:67]
	global_load_dword v155, v[162:163], off offset:2048 nt
	v_lshl_add_u64 v[162:163], v[162:163], 0, s[66:67]
	global_load_dword v156, v[162:163], off offset:2048 nt
	v_lshl_add_u64 v[162:163], v[162:163], 0, s[66:67]
	global_load_dword v157, v[162:163], off offset:2048 nt
	s_waitcnt vmcnt(0)
	v_lshlrev_b32_e32 v14, 16, v24
	v_and_b32_e32 v15, 0xffff0000, v24
	v_lshlrev_b32_e32 v22, 16, v23
	v_and_b32_e32 v23, 0xffff0000, v23
	v_pk_fma_f32 v[14:15], v[8:9], v[14:15], v[12:13]
	v_lshlrev_b32_e32 v20, 16, v21
	v_and_b32_e32 v21, 0xffff0000, v21
	v_pk_fma_f32 v[14:15], v[4:5], v[22:23], v[14:15]
	v_lshlrev_b32_e32 v18, 16, v19
	v_and_b32_e32 v19, 0xffff0000, v19
	v_pk_fma_f32 v[14:15], v[6:7], v[20:21], v[14:15]
	v_and_b32_e32 v29, 0xfe, v17
	v_pk_fma_f32 v[24:25], v[10:11], v[18:19], v[14:15]
	s_lshl_b32 s58, s8, 1
	v_mul_f32_e32 v14, 0xbfb8aa3b, v24
	v_exp_f32_e32 v17, v14
	v_mul_f32_e32 v14, 0xbfb8aa3b, v25
	v_exp_f32_e32 v31, v14
	s_add_u32 s8, s16, s58
	v_add_f32_e32 v17, 1.0, v17
	v_rcp_f32_e32 v46, v17
	v_add_f32_e32 v17, 1.0, v31
	v_rcp_f32_e32 v47, v17
	s_addc_u32 s9, s17, 0
	v_lshlrev_b32_e32 v66, 1, v16
	s_add_u32 s64, s6, s58
	v_cmp_lt_u32_e32 vcc, s72, v29
	v_lshl_add_u64 v[14:15], s[8:9], 0, v[66:67]
	v_mad_u32_u24 v31, v16, s73, 0
	s_addc_u32 s65, s7, 0
	v_pk_mul_f32 v[24:25], v[24:25], v[46:47]
	s_and_saveexec_b64 s[8:9], vcc
	s_xor_b64 s[66:67], exec, s[8:9]
	s_cbranch_execz .LBB0_438
	v_pk_mul_f32 v[16:17], v[24:25], s[60:61] op_sel_hi:[1,0]
	s_nop 0
	v_bfe_u32 v24, v16, 16, 1
	v_add3_u32 v24, v16, v24, s75
	v_bfe_u32 v25, v17, 16, 1
	v_lshrrev_b32_e32 v16, 16, v24
	v_add3_u32 v25, v17, v25, s75
	v_and_or_b32 v46, v25, s71, v16
	v_add_u32_e32 v16, s82, v2
	v_ashrrev_i32_e32 v17, 31, v16
	v_lshlrev_b64 v[16:17], 10, v[16:17]
	v_lshl_add_u64 v[16:17], v[14:15], 0, v[16:17]
	global_store_dword v[16:17], v46, off
	v_lshl_add_u32 v16, v2, 1, v31
	ds_write_b16_d16_hi v16, v24 offset:1024
	ds_write_b16_d16_hi v16, v25 offset:1168

.LBB0_509:
	v_lshl_add_u64 v[6:7], v[2:3], 0, s[64:65]
	v_add_co_u32_e32 v8, vcc, 0x6800000, v6
	s_add_u32 s64, s64, 0xc000
	s_nop 0
	v_addc_co_u32_e32 v9, vcc, 0, v7, vcc
	v_add_co_u32_e32 v10, vcc, 0x6803000, v6
	global_load_dword v5, v[8:9], off offset:2048 nt
	s_nop 0
	v_addc_co_u32_e32 v11, vcc, 0, v7, vcc
	global_load_dword v10, v[10:11], off offset:2048 nt
	v_add_co_u32_e32 v8, vcc, 0x6806000, v6
	s_addc_u32 s65, s65, 0
	s_nop 0
	v_addc_co_u32_e32 v9, vcc, 0, v7, vcc
	v_add_co_u32_e32 v6, vcc, 0x6809000, v6
	global_load_dword v11, v[8:9], off offset:2048 nt
	s_nop 0
	v_addc_co_u32_e32 v7, vcc, 0, v7, vcc
	global_load_dword v12, v[6:7], off offset:2048 nt
	ds_read_b128 v[6:9], v4
	v_add_u32_e32 v4, 16, v4
	s_cmp_eq_u32 s64, 0x30000
	s_waitcnt vmcnt(3)
	v_lshlrev_b32_e32 v13, 16, v5
	v_and_b32_e32 v5, 0xffff0000, v5
	s_waitcnt lgkmcnt(0)
	v_mul_f32_e32 v13, v6, v13
	v_mul_f32_e32 v5, v6, v5
	s_waitcnt vmcnt(2)
	v_lshlrev_b32_e32 v6, 16, v10
	v_and_b32_e32 v10, 0xffff0000, v10
	v_bfe_u32 v14, v13, 16, 1
	v_mul_f32_e32 v6, v7, v6
	v_mul_f32_e32 v7, v7, v10
	v_bfe_u32 v15, v5, 16, 1
	v_add3_u32 v13, v13, v14, s75
	s_waitcnt vmcnt(1)
	v_lshlrev_b32_e32 v10, 16, v11
	v_and_b32_e32 v11, 0xffff0000, v11
	v_bfe_u32 v14, v6, 16, 1
	v_mul_f32_e32 v10, v8, v10
	v_mul_f32_e32 v8, v8, v11
	s_waitcnt vmcnt(0)
	v_lshlrev_b32_e32 v11, 16, v12
	v_and_b32_e32 v12, 0xffff0000, v12
	v_add3_u32 v5, v5, v15, s75
	v_bfe_u32 v15, v7, 16, 1
	v_add3_u32 v6, v6, v14, s75
	v_bfe_u32 v14, v10, 16, 1
	v_mul_f32_e32 v11, v9, v11
	v_mul_f32_e32 v9, v9, v12
	v_add3_u32 v7, v7, v15, s75
	v_bfe_u32 v15, v8, 16, 1
	v_add3_u32 v10, v10, v14, s75
	v_bfe_u32 v14, v11, 16, 1
	v_perm_b32 v6, v6, v13, s80
	v_bfe_u32 v13, v9, 16, 1
	v_add3_u32 v12, v8, v15, s75
	v_perm_b32 v8, v7, v5, s80
	v_add3_u32 v5, v11, v14, s75
	v_add3_u32 v9, v9, v13, s75
	v_perm_b32 v7, v5, v10, s80
	v_perm_b32 v9, v9, v12, s80
	ds_write2_b64 v1, v[6:7], v[8:9] offset1:18
	v_add_u32_e32 v1, 8, v1
	s_cbranch_scc0 .LBB0_509

.LBB0_647:
	v_mov_b32_e32 v86, v0
	v_mov_b32_e32 v1, v0
	s_mov_b32 s2, 8
	s_ashr_i32 s3, s2, 31
	s_lshl_b64 s[2:3], s[2:3], 3
	s_add_u32 s38, s0, s2
	s_addc_u32 s39, s1, s3
	s_lshl_b32 s2, s36, 6
	s_ashr_i32 s37, s36, 31
	s_lshl_b32 s4, s36, 4
	s_and_b32 s5, s2, 0x7c0
	s_lshl_b64 s[2:3], s[36:37], 16
	s_add_u32 s2, s16, s2
	v_and_or_b32 v82, v1, 31, s20
	s_addc_u32 s3, s17, s3
	v_lshlrev_b64 v[2:3], 8, v[82:83]
	v_lshrrev_b32_e32 v4, 1, v1
	v_lshl_add_u64 v[2:3], s[2:3], 0, v[2:3]
	v_and_b32_e32 v82, 16, v4
	v_lshl_add_u64 v[2:3], v[2:3], 0, v[82:83]
	s_and_b32 s3, s4, 0xfffff800
	s_lshl_b32 s4, s36, 7
	global_load_dwordx4 v[62:65], v[2:3], off nt
	global_load_dwordx4 v[58:61], v[2:3], off offset:32 nt
	global_load_dwordx4 v[54:57], v[2:3], off offset:64 nt
	global_load_dwordx4 v[50:53], v[2:3], off offset:96 nt
	global_load_dwordx4 v[30:33], v[2:3], off offset:128 nt
	global_load_dwordx4 v[26:29], v[2:3], off offset:160 nt
	global_load_dwordx4 v[22:25], v[2:3], off offset:192 nt
	global_load_dwordx4 v[18:21], v[2:3], off offset:224 nt
	s_or_b32 s40, s3, s5
	s_ashr_i32 s5, s4, 31
	s_bfe_u32 s2, s36, 0x20005
	s_lshl_b64 s[4:5], s[4:5], 2
	s_add_u32 s4, s21, s4
	v_and_b32_e32 v87, 7, v86
	s_addc_u32 s5, s22, s5
	v_lshlrev_b32_e32 v66, 6, v87
	global_load_dwordx4 v[2:5], v66, s[4:5] offset:48 nt
	global_load_dwordx4 v[6:9], v66, s[4:5] offset:32 nt
	global_load_dwordx4 v[10:13], v66, s[4:5] offset:16 nt
	global_load_dwordx4 v[14:17], v66, s[4:5] nt
	v_and_b32_e32 v85, 63, v1
	s_andn2_b64 vcc, exec, s[28:29]
	v_mov_b32_e32 v38, 0
	v_mov_b32_e32 v40, 0
	v_mov_b32_e32 v39, 0
	s_cbranch_vccnz .LBB0_649
	v_or_b32_e32 v34, s40, v85
	s_lshl_b64 s[4:5], s[36:37], 2
	v_ashrrev_i32_e32 v35, 31, v34
	s_add_u32 s4, s18, s4
	v_lshlrev_b64 v[34:35], 5, v[34:35]
	s_addc_u32 s5, s19, s5
	v_lshl_add_u64 v[34:35], s[12:13], 0, v[34:35]
	s_lshl_b32 s26, s2, 2
	v_lshl_add_u64 v[34:35], v[34:35], 0, s[26:27]
	global_load_dword v39, v[34:35], off nt
	global_load_dword v40, v[34:35], off offset:16 nt
	global_load_dword v38, v88, s[4:5] nt
.LBB0_649:
	v_cmp_gt_u32_e32 vcc, s62, v86
	v_lshlrev_b32_e32 v41, 4, v86
	v_bfe_u32 v1, v86, 4, 6
	v_cndmask_b32_e32 v82, v93, v94, vcc
	v_lshl_add_u64 v[34:35], s[18:19], 0, v[82:83]
	v_and_b32_e32 v82, 0xf0, v41
	v_add_u32_e32 v41, 0x200, v86
	v_or_b32_e32 v36, s40, v1
	v_bfe_u32 v48, v41, 4, 6
	v_ashrrev_i32_e32 v37, 31, v36
	s_lshl_b32 s26, s2, 8
	v_cmp_gt_u32_e64 s[2:3], s62, v41
	v_or_b32_e32 v44, s40, v48
	v_lshlrev_b64 v[36:37], 10, v[36:37]
	v_cndmask_b32_e64 v42, v93, v94, s[2:3]
	v_mov_b32_e32 v43, v83
	v_ashrrev_i32_e32 v45, 31, v44
	v_lshl_add_u64 v[34:35], v[34:35], 0, v[36:37]
	v_lshl_add_u64 v[42:43], s[18:19], 0, v[42:43]
	v_lshlrev_b64 v[44:45], 10, v[44:45]
	v_lshl_add_u64 v[34:35], v[34:35], 0, s[26:27]
	v_lshl_add_u64 v[42:43], v[42:43], 0, v[44:45]
	v_lshl_add_u64 v[34:35], v[34:35], 0, v[82:83]
	v_lshl_add_u64 v[42:43], v[42:43], 0, s[26:27]
	v_cmp_lt_u32_e64 s[4:5], s66, v86
	v_lshl_add_u64 v[42:43], v[42:43], 0, v[82:83]
	global_load_dwordx4 v[44:47], v[34:35], off nt
	global_load_dwordx4 v[68:71], v[42:43], off nt
	v_cndmask_b32_e64 v34, v93, v94, s[4:5]
	v_mov_b32_e32 v35, v83
	v_lshl_add_u64 v[34:35], s[18:19], 0, v[34:35]
	v_lshl_add_u64 v[34:35], v[34:35], 0, v[36:37]
	v_add_u32_e32 v36, 0x600, v86
	v_bfe_u32 v49, v36, 4, 6
	v_cmp_gt_u32_e64 s[6:7], s62, v36
	v_or_b32_e32 v42, s40, v49
	v_mov_b32_e32 v37, v83
	v_cndmask_b32_e64 v36, v93, v94, s[6:7]
	v_ashrrev_i32_e32 v43, 31, v42
	v_lshl_add_u64 v[36:37], s[18:19], 0, v[36:37]
	v_lshlrev_b64 v[42:43], 10, v[42:43]
	v_lshl_add_u64 v[34:35], v[34:35], 0, s[26:27]
	v_lshl_add_u64 v[36:37], v[36:37], 0, v[42:43]
	v_lshl_add_u64 v[34:35], v[34:35], 0, v[82:83]
	v_lshl_add_u64 v[36:37], v[36:37], 0, s[26:27]
	v_lshl_add_u64 v[36:37], v[36:37], 0, v[82:83]
	global_load_dwordx4 v[72:75], v[34:35], off nt
	global_load_dwordx4 v[76:79], v[36:37], off nt
	v_mov_b32_e32 v35, s64
	v_mov_b32_e32 v36, s63
	v_ashrrev_i32_e32 v98, 3, v86
	v_lshlrev_b32_e32 v37, 1, v86
	v_cndmask_b32_e32 v42, v35, v36, vcc
	v_mul_u32_u24_e32 v1, 0x110, v1
	v_cndmask_b32_e64 v43, v35, v36, s[4:5]
	v_and_b32_e32 v41, 0xfe, v37
	v_lshlrev_b32_e32 v37, 1, v98
	s_load_dwordx2 s[38:39], s[38:39], 0x0
	v_add3_u32 v67, v42, v1, v82
	v_cndmask_b32_e64 v80, v35, v36, s[2:3]
	v_add3_u32 v1, v43, v1, v82
	v_cndmask_b32_e64 v36, v35, v36, s[6:7]
	v_mul_u32_u24_e32 v43, 0x110, v49
	v_mad_u32_u24 v35, v41, s67, 0
	v_and_b32_e32 v42, 0xffffffe0, v37
	v_mul_u32_u24_e32 v48, 0x110, v48
	v_add3_u32 v36, v36, v43, v82
	v_add_u32_e32 v43, v35, v42
	v_add3_u32 v37, v80, v48, v82
	v_add_u32_e32 v48, 0x9000, v43
	v_add_u32_e32 v49, 0x901e, v43
	v_add_u32_e32 v80, 0x9090, v43
	v_add_u32_e32 v43, 0x90ae, v43
	v_cmp_ge_u32_e32 vcc, v49, v48
	v_cmp_ge_u32_e64 s[2:3], v43, v80
	v_and_b32_e32 v34, -16, v98
	s_and_b64 s[2:3], vcc, s[2:3]
	s_lshl_b32 s6, s26, 1
	s_add_u32 s6, s10, s6
	s_addc_u32 s7, s11, 0
	v_lshlrev_b32_e32 v158, 2, v0
	v_and_b32_e32 v158, 0x1fc, v158
	v_mov_b32_e32 v159, 0
	v_lshl_add_u64 v[160:161], s[6:7], 0, v[158:159]
	v_ashrrev_i32_e32 v158, 3, v0
	v_and_b32_e32 v158, -16, v158
	v_add_u32_e32 v158, s40, v158
	v_mad_i64_i32 v[162:163], s[6:7], v158, s68, v[160:161]
	s_mov_b32 s6, 0x3000
	s_mov_b32 s7, 0
	global_load_dword v142, v[162:163], off offset:2048 nt
	v_lshl_add_u64 v[162:163], v[162:163], 0, s[6:7]
	global_load_dword v143, v[162:163], off offset:2048 nt
	v_lshl_add_u64 v[162:163], v[162:163], 0, s[6:7]
	global_load_dword v144, v[162:163], off offset:2048 nt
	v_lshl_add_u64 v[162:163], v[162:163], 0, s[6:7]
	global_load_dword v145, v[162:163], off offset:2048 nt
	v_lshl_add_u64 v[162:163], v[162:163], 0, s[6:7]
	global_load_dword v146, v[162:163], off offset:2048 nt
	v_lshl_add_u64 v[162:163], v[162:163], 0, s[6:7]
	global_load_dword v147, v[162:163], off offset:2048 nt
	v_lshl_add_u64 v[162:163], v[162:163], 0, s[6:7]
	global_load_dword v148, v[162:163], off offset:2048 nt
	v_lshl_add_u64 v[162:163], v[162:163], 0, s[6:7]
	global_load_dword v149, v[162:163], off offset:2048 nt
	v_lshl_add_u64 v[162:163], v[162:163], 0, s[6:7]
	global_load_dword v150, v[162:163], off offset:2048 nt
	v_lshl_add_u64 v[162:163], v[162:163], 0, s[6:7]
	global_load_dword v151, v[162:163], off offset:2048 nt
	v_lshl_add_u64 v[162:163], v[162:163], 0, s[6:7]
	global_load_dword v152, v[162:163], off offset:2048 nt
	v_lshl_add_u64 v[162:163], v[162:163], 0, s[6:7]
	global_load_dword v153, v[162:163], off offset:2048 nt
	v_lshl_add_u64 v[162:163], v[162:163], 0, s[6:7]
	global_load_dword v154, v[162:163], off offset:2048 nt
	v_lshl_add_u64 v[162:163], v[162:163], 0, s[6:7]
	global_load_dword v155, v[162:163], off offset:2048 nt
	v_lshl_add_u64 v[162:163], v[162:163], 0, s[6:7]
	global_load_dword v156, v[162:163], off offset:2048 nt
	v_lshl_add_u64 v[162:163], v[162:163], 0, s[6:7]
	global_load_dword v157, v[162:163], off offset:2048 nt
	s_waitcnt vmcnt(0)
	ds_write_b128 v67, v[44:47]
	ds_write_b128 v37, v[68:71]
	ds_write_b128 v1, v[72:75]
	ds_write_b128 v36, v[76:79]
	s_and_saveexec_b64 s[4:5], s[2:3]
	s_xor_b64 s[2:3], exec, s[4:5]
	s_cbranch_execz .LBB0_652
	s_lshl_b32 s6, s26, 1
	s_add_u32 s6, s10, s6
	s_addc_u32 s7, s11, 0
	v_lshlrev_b32_e32 v82, 1, v41
	v_mov_b32_e32 v1, v34
	s_mov_b32 s4, s40
	s_mov_b32 s5, 1
	v_lshl_add_u64 v[36:37], s[6:7], 0, v[82:83]
	s_mov_b32 s6, 0
	s_mov_b32 s7, 16
	v_or_b32_e32 v67, s6, v34
	v_or_b32_e32 v41, s5, v1
	s_add_i32 s37, s5, 2
	s_add_i32 s41, s6, 2
	s_add_i32 s82, s5, 4
	s_add_i32 s83, s6, 4
	v_add_u32_e32 v42, s40, v67
	s_add_i32 s84, s5, 6
	s_add_i32 s85, s6, 6
	v_add_u32_e32 v41, s4, v41
	v_or_b32_e32 v46, s37, v1
	v_or_b32_e32 v72, s41, v34
	v_or_b32_e32 v47, s82, v1
	v_or_b32_e32 v73, s83, v34
	v_mad_i64_i32 v[42:43], s[82:83], v42, s68, v[36:37]
	v_or_b32_e32 v48, s84, v1
	v_or_b32_e32 v74, s85, v34
	v_mad_i64_i32 v[44:45], s[82:83], v41, s68, v[36:37]
	v_add_u32_e32 v41, s4, v46
	v_add_u32_e32 v46, s40, v72
	v_add_u32_e32 v49, s4, v47
	v_add_u32_e32 v47, s40, v73
	v_mov_b32_e32 v75, v142
	v_mov_b32_e32 v76, v143
	v_add_u32_e32 v70, s4, v48
	v_add_u32_e32 v68, s40, v74
	v_mad_i64_i32 v[42:43], s[82:83], v46, s68, v[36:37]
	v_mad_i64_i32 v[44:45], s[82:83], v41, s68, v[36:37]
	v_mad_i64_i32 v[46:47], s[82:83], v47, s68, v[36:37]
	v_mad_i64_i32 v[48:49], s[82:83], v49, s68, v[36:37]
	v_mad_i64_i32 v[68:69], s[82:83], v68, s68, v[36:37]
	v_mad_i64_i32 v[70:71], s[82:83], v70, s68, v[36:37]
	v_mov_b32_e32 v43, v144
	s_nop 0
	v_mov_b32_e32 v44, v145
	s_nop 0
	v_mov_b32_e32 v45, v146
	s_nop 0
	v_mov_b32_e32 v46, v147
	v_mov_b32_e32 v47, v148
	s_nop 0
	v_mov_b32_e32 v48, v149
	v_lshl_add_u32 v49, v67, 1, v35
	s_add_i32 s6, s6, 8
	s_add_i32 s5, s5, 8
	s_add_i32 s7, s7, -8
	v_add_u32_e32 v49, 0x9000, v49
	v_lshl_add_u32 v67, v72, 1, v35
	s_cmp_lg_u32 s7, 0
	v_lshl_add_u32 v68, v73, 1, v35
	v_lshl_add_u32 v69, v74, 1, v35
	v_add_u32_e32 v67, 0x9000, v67
	v_add_u32_e32 v68, 0x9000, v68
	v_add_u32_e32 v69, 0x9000, v69
	v_perm_b32 v70, v76, v75, s69
	v_perm_b32 v71, v76, v75, s70
	ds_write2_b32 v49, v70, v71 offset1:36
	v_perm_b32 v49, v44, v43, s69
	v_perm_b32 v43, v44, v43, s70
	v_perm_b32 v44, v46, v45, s69
	v_perm_b32 v45, v46, v45, s70
	v_perm_b32 v46, v48, v47, s69
	v_perm_b32 v47, v48, v47, s70
	ds_write2_b32 v67, v49, v43 offset1:36
	ds_write2_b32 v68, v44, v45 offset1:36
	ds_write2_b32 v69, v46, v47 offset1:36
	v_or_b32_e32 v67, s6, v34
	v_or_b32_e32 v41, s5, v1
	s_add_i32 s37, s5, 2
	s_add_i32 s41, s6, 2
	s_add_i32 s82, s5, 4
	s_add_i32 s83, s6, 4
	v_add_u32_e32 v42, s40, v67
	s_add_i32 s84, s5, 6
	s_add_i32 s85, s6, 6
	v_add_u32_e32 v41, s4, v41
	v_or_b32_e32 v46, s37, v1
	v_or_b32_e32 v72, s41, v34
	v_or_b32_e32 v47, s82, v1
	v_or_b32_e32 v73, s83, v34
	v_mad_i64_i32 v[42:43], s[82:83], v42, s68, v[36:37]
	v_or_b32_e32 v48, s84, v1
	v_or_b32_e32 v74, s85, v34
	v_mad_i64_i32 v[44:45], s[82:83], v41, s68, v[36:37]
	v_add_u32_e32 v41, s4, v46
	v_add_u32_e32 v46, s40, v72
	v_add_u32_e32 v49, s4, v47
	v_add_u32_e32 v47, s40, v73
	v_mov_b32_e32 v75, v150
	v_mov_b32_e32 v76, v151
	v_add_u32_e32 v70, s4, v48
	v_add_u32_e32 v68, s40, v74
	v_mad_i64_i32 v[42:43], s[82:83], v46, s68, v[36:37]
	v_mad_i64_i32 v[44:45], s[82:83], v41, s68, v[36:37]
	v_mad_i64_i32 v[46:47], s[82:83], v47, s68, v[36:37]
	v_mad_i64_i32 v[48:49], s[82:83], v49, s68, v[36:37]
	v_mad_i64_i32 v[68:69], s[82:83], v68, s68, v[36:37]
	v_mad_i64_i32 v[70:71], s[82:83], v70, s68, v[36:37]
	v_mov_b32_e32 v43, v152
	s_nop 0
	v_mov_b32_e32 v44, v153
	s_nop 0
	v_mov_b32_e32 v45, v154
	s_nop 0
	v_mov_b32_e32 v46, v155
	v_mov_b32_e32 v47, v156
	s_nop 0
	v_mov_b32_e32 v48, v157
	v_lshl_add_u32 v49, v67, 1, v35
	s_add_i32 s6, s6, 8
	s_add_i32 s5, s5, 8
	s_add_i32 s7, s7, -8
	v_add_u32_e32 v49, 0x9000, v49
	v_lshl_add_u32 v67, v72, 1, v35
	s_cmp_lg_u32 s7, 0
	v_lshl_add_u32 v68, v73, 1, v35
	v_lshl_add_u32 v69, v74, 1, v35
	v_add_u32_e32 v67, 0x9000, v67
	v_add_u32_e32 v68, 0x9000, v68
	v_add_u32_e32 v69, 0x9000, v69
	v_perm_b32 v70, v76, v75, s69
	v_perm_b32 v71, v76, v75, s70
	ds_write2_b32 v49, v70, v71 offset1:36
	v_perm_b32 v49, v44, v43, s69
	v_perm_b32 v43, v44, v43, s70
	v_perm_b32 v44, v46, v45, s69
	v_perm_b32 v45, v46, v45, s70
	v_perm_b32 v46, v48, v47, s69
	v_perm_b32 v47, v48, v47, s70
	ds_write2_b32 v67, v49, v43 offset1:36
	ds_write2_b32 v68, v44, v45 offset1:36
	ds_write2_b32 v69, v46, v47 offset1:36

.LBB0_654:
	v_lshl_add_u64 v[36:37], v[34:35], 0, s[4:5]
	v_add_co_u32_e32 v42, vcc, 0x6800000, v36
	s_add_u32 s4, s4, 0xc000
	s_nop 0
	v_addc_co_u32_e32 v43, vcc, 0, v37, vcc
	v_add_co_u32_e32 v44, vcc, 0x6803000, v36
	s_addc_u32 s5, s5, 0
	s_nop 0
	v_addc_co_u32_e32 v45, vcc, 0, v37, vcc
	v_add_co_u32_e32 v46, vcc, 0x6806000, v36
	global_load_dword v41, v[42:43], off offset:2048 nt
	s_nop 0
	global_load_dword v42, v[44:45], off offset:2048 nt
	v_addc_co_u32_e32 v47, vcc, 0, v37, vcc
	v_add_co_u32_e32 v36, vcc, 0x6809000, v36
	s_cmp_eq_u32 s4, 0x30000
	s_nop 0
	v_addc_co_u32_e32 v37, vcc, 0, v37, vcc
	global_load_dword v43, v[46:47], off offset:2048 nt
	global_load_dword v44, v[36:37], off offset:2048 nt
	s_waitcnt vmcnt(2)
	v_perm_b32 v36, v42, v41, s69
	v_perm_b32 v42, v42, v41, s70
	s_waitcnt vmcnt(0)
	v_perm_b32 v37, v44, v43, s69
	v_perm_b32 v43, v44, v43, s70
	ds_write2_b64 v1, v[36:37], v[42:43] offset1:18
	v_add_u32_e32 v1, 8, v1
	s_cbranch_scc0 .LBB0_654

.LBB0_697:
	v_lshl_add_u32 v1, v82, 4, 0
	v_mad_u32_u24 v76, v99, s65, v1
	s_waitcnt lgkmcnt(1)
	ds_read_b128 v[2:5], v76 offset:2048
	ds_read_b128 v[68:71], v76 offset:2080
	v_add_u32_e32 v84, s40, v98
	s_lshl_b32 s6, s26, 1
	s_mov_b32 s7, s27
	s_waitcnt lgkmcnt(1)
	v_mfma_f32_32x32x16_bf16 v[34:49], v[2:5], v[62:65], 0
	ds_read_b128 v[2:5], v76 offset:10752
	ds_read_b128 v[72:75], v76 offset:10784
	v_mov_b32_e32 v67, v83
	s_waitcnt lgkmcnt(1)
	v_mfma_f32_32x32x16_bf16 v[2:17], v[2:5], v[62:65], 0
	v_mfma_f32_32x32x16_bf16 v[34:49], v[68:71], v[58:61], v[34:49]
	s_waitcnt lgkmcnt(0)
	v_mfma_f32_32x32x16_bf16 v[2:17], v[72:75], v[58:61], v[2:17]
	ds_read_b128 v[58:61], v76 offset:2112
	ds_read_b128 v[62:65], v76 offset:2144
	s_waitcnt lgkmcnt(1)
	v_mfma_f32_32x32x16_bf16 v[34:49], v[58:61], v[54:57], v[34:49]
	ds_read_b128 v[58:61], v76 offset:10816
	ds_read_b128 v[68:71], v76 offset:10848
	s_waitcnt lgkmcnt(1)
	v_mfma_f32_32x32x16_bf16 v[2:17], v[58:61], v[54:57], v[2:17]
	v_mfma_f32_32x32x16_bf16 v[34:49], v[62:65], v[50:53], v[34:49]
	s_waitcnt lgkmcnt(0)
	v_mfma_f32_32x32x16_bf16 v[2:17], v[68:71], v[50:53], v[2:17]
	ds_read_b128 v[50:53], v76 offset:2176
	ds_read_b128 v[54:57], v76 offset:2208
	s_waitcnt lgkmcnt(1)
	v_mfma_f32_32x32x16_bf16 v[34:49], v[50:53], v[30:33], v[34:49]
	ds_read_b128 v[50:53], v76 offset:10880
	ds_read_b128 v[58:61], v76 offset:10912
	s_waitcnt lgkmcnt(1)
	v_mfma_f32_32x32x16_bf16 v[2:17], v[50:53], v[30:33], v[2:17]
	v_mov_b64_e32 v[30:31], s[10:11]
	v_mfma_f32_32x32x16_bf16 v[34:49], v[54:57], v[26:29], v[34:49]
	v_mad_i64_i32 v[54:55], s[2:3], v84, s68, v[30:31]
	s_waitcnt lgkmcnt(0)
	v_mfma_f32_32x32x16_bf16 v[2:17], v[58:61], v[26:29], v[2:17]
	ds_read_b128 v[26:29], v76 offset:2240
	ds_read_b128 v[30:33], v76 offset:10944
	ds_read_b128 v[50:53], v76 offset:2272
	s_waitcnt lgkmcnt(2)
	v_mfma_f32_32x32x16_bf16 v[34:49], v[26:29], v[22:25], v[34:49]
	v_lshl_add_u64 v[26:27], v[54:55], 0, s[6:7]
	v_lshl_add_u64 v[54:55], v[26:27], 0, v[66:67]
	v_lshl_add_u64 v[56:57], v[54:55], 0, s[34:35]
	ds_read_b128 v[26:29], v76 offset:10976
	s_waitcnt lgkmcnt(2)
	v_mfma_f32_32x32x16_bf16 v[2:17], v[30:33], v[22:25], v[2:17]
	v_add_co_u32_e32 v22, vcc, 0x1000, v54
	s_nop 1
	v_addc_co_u32_e32 v23, vcc, 0, v55, vcc
	global_load_dwordx4 v[78:81], v[22:23], off nt
	global_load_dwordx4 v[66:69], v[56:57], off offset:48 nt
	global_load_dwordx4 v[70:73], v[56:57], off offset:32 nt
	global_load_dwordx4 v[74:77], v[56:57], off offset:16 nt
	s_waitcnt lgkmcnt(1)
	v_mfma_f32_32x32x16_bf16 v[34:49], v[50:53], v[18:21], v[34:49]
	s_waitcnt lgkmcnt(0)
	s_barrier
	v_or_b32_e32 v22, s20, v99
	v_mul_lo_u32 v22, v22, s67
	v_add3_u32 v22, 0, v22, v100
	v_add_u32_e32 v112, 0x9000, v22
	v_mfma_f32_32x32x16_bf16 v[2:17], v[26:29], v[18:21], v[2:17]
	v_lshl_add_u32 v18, v85, 4, 0
	v_add_u32_e32 v85, 0x12000, v18
	ds_read_b128 v[18:21], v85
	ds_read2_b64 v[22:25], v112 offset1:2
	ds_read_b128 v[26:29], v85 offset:1024
	ds_read2_b64 v[100:103], v112 offset0:4 offset1:6
	ds_read_b128 v[104:107], v85 offset:3072
	v_cmp_gt_i32_e32 vcc, 64, v86
	s_waitcnt lgkmcnt(3)
	v_mfma_f32_32x32x16_bf16 v[50:65], v[18:21], v[22:25], 0
	ds_read_b128 v[18:21], v85 offset:2048
	s_waitcnt lgkmcnt(2)
	v_mfma_f32_32x32x16_bf16 v[50:65], v[26:29], v[100:103], v[50:65]
	s_waitcnt lgkmcnt(0)
	v_mfma_f32_32x32x16_bf16 v[18:33], v[18:21], v[22:25], 0
	v_mfma_f32_32x32x16_bf16 v[18:33], v[104:107], v[100:103], v[18:33]
	ds_read_b128 v[100:103], v85 offset:4096
	ds_read2_b64 v[104:107], v112 offset0:8 offset1:10
	ds_read_b128 v[108:111], v85 offset:5120
	s_waitcnt lgkmcnt(1)
	v_mfma_f32_32x32x16_bf16 v[18:33], v[100:103], v[104:107], v[18:33]
	ds_read2_b64 v[100:103], v112 offset0:12 offset1:14
	s_waitcnt lgkmcnt(0)
	v_mfma_f32_32x32x16_bf16 v[18:33], v[108:111], v[100:103], v[18:33]
	s_and_saveexec_b64 s[4:5], vcc
	s_cbranch_execz .LBB0_701
	v_lshl_add_u32 v85, v86, 2, 0
	ds_read_b32 v100, v85 offset:1536
	v_cmp_lt_i32_e64 s[2:3], 31, v86
	s_and_saveexec_b64 s[40:41], s[2:3]
	s_cbranch_execz .LBB0_700
	ds_read_b32 v101, v85 offset:1664
	s_waitcnt lgkmcnt(0)
	v_add_f32_e32 v100, v100, v101
